# lever 4 (static wave priority): in P2 the attention-preferring waves run at user priority 1 over the conversion waves sharing their SIMD; reset at the P2->P3 seam
# baseline (speedup 1.0000x reference)
.LBB0_416:
	s_cmp_lt_i32 s80, 3
	s_cselect_b64 s[4:5], -1, 0
	s_add_u32 s2, s90, 0x1800000
	s_addc_u32 s3, s91, 0
	s_add_u32 s66, s90, 0x5800000
	s_addc_u32 s67, s91, 0
	s_add_u32 s6, s90, 0x1b000000
	s_addc_u32 s7, s91, 0
	v_writelane_b32 v255, s6, 50
	s_and_b64 s[4:5], s[4:5], s[0:1]
	s_mov_b32 s19, 0
	v_writelane_b32 v255, s7, 51
	s_mov_b32 s6, 1
	s_cmp_gt_i32 s6, 0
	s_cselect_b64 s[0:1], -1, 0
	s_and_b64 s[0:1], s[4:5], s[0:1]
	v_writelane_b32 v255, s6, 43
	s_andn2_b64 vcc, exec, s[0:1]
	s_cbranch_vccnz .LBB0_819
	v_writelane_b32 v255, s4, 52
	s_add_u32 s10, s90, 0x1e000000
	s_addc_u32 s11, s91, 0
	v_writelane_b32 v255, s5, 53
	s_add_u32 s14, s90, 0x15800000
	v_readlane_b32 s0, v255, 2
	s_addc_u32 s15, s91, 0
	s_addk_i32 s0, 0x7ff
	s_ashr_i32 s1, s0, 31
	v_readlane_b32 s4, v255, 19
	s_abs_i32 s0, s0
	s_xor_b32 s1, s1, s4
	s_mul_hi_u32 s4, s0, s96
	s_mul_i32 s5, s4, s94
	s_sub_i32 s0, s0, s5
	s_add_i32 s5, s4, 1
	s_sub_i32 s6, s0, s94
	s_cmp_ge_u32 s0, s94
	s_cselect_b32 s4, s5, s4
	s_cselect_b32 s0, s6, s0
	s_add_i32 s5, s4, 1
	s_cmp_ge_u32 s0, s94
	s_cselect_b32 s0, s5, s4
	s_xor_b32 s0, s0, s1
	s_sub_i32 s35, s0, s1
	v_readlane_b32 s0, v255, 18
	v_readlane_b32 s7, v255, 20
	s_mulk_i32 s0, 0x2100
	s_add_i32 s79, s35, s33
	s_add_i32 s9, s7, s33
	s_add_i32 s0, s0, 0
	s_cmp_gt_i32 s79, 0
	s_cselect_b64 s[4:5], -1, 0
	v_writelane_b32 v255, s4, 41
	v_lshrrev_b32_e32 v142, 3, v1
	s_waitcnt vmcnt(0)
	v_and_b32_e32 v4, 7, v0
	v_writelane_b32 v255, s5, 42
	v_mul_u32_u24_e32 v2, 0x84, v142
	v_readlane_b32 s1, v255, 27
	v_readlane_b32 s6, v255, 8
	s_cmpk_lt_u32 s1, 0x140
	s_mul_i32 s1, s7, s6
	s_cselect_b64 s[82:83], -1, 0
	s_cbranch_scc0 .Lp2prio_skip
	s_setprio 1
.Lp2prio_skip:
	s_sub_i32 s22, s1, s33
	v_lshlrev_b32_e32 v5, 4, v4
	s_mul_i32 s23, s33, s6
	s_add_u32 s84, s90, 0xe00400
	v_add3_u32 v143, s0, v2, v5
	v_lshlrev_b32_e32 v146, 3, v4
	v_mul_u32_u24_e32 v2, 0x420, v4
	v_lshlrev_b32_e32 v4, 2, v142
	s_addc_u32 s85, s91, 0
	v_add3_u32 v145, s0, v2, v4
	s_sub_i32 s0, s23, s35
	v_writelane_b32 v255, s0, 58
	s_mul_i32 s0, s35, s6
	s_addk_i32 s0, 0x1000
	v_writelane_b32 v255, s0, 57
	v_writelane_b32 v255, s14, 39
	v_mov_b32_e32 v3, 0
	v_and_b32_e32 v149, 15, v0
	v_writelane_b32 v255, s15, 40
	v_lshlrev_b32_e32 v160, 6, v149
	v_mov_b32_e32 v161, v3
	v_writelane_b32 v255, s10, 60
	v_and_b32_e32 v2, 48, v1
	v_and_b32_e32 v154, 48, v0
	v_writelane_b32 v255, s11, 61
	v_lshl_add_u64 v[4:5], s[10:11], 0, v[160:161]
	v_lshl_add_u64 v[164:165], v[4:5], 0, v[2:3]
	v_lshrrev_b32_e32 v4, 2, v0
	v_readlane_b32 s0, v255, 31
	v_mov_b32_e32 v155, v3
	v_and_b32_e32 v166, 12, v4
	v_readlane_b32 s1, v255, 32
	v_lshl_add_u64 v[4:5], s[90:91], 0, v[160:161]
	v_lshlrev_b32_e32 v151, 4, v149
	v_lshl_add_u64 v[168:169], s[0:1], 0, v[154:155]
	v_lshl_add_u64 v[4:5], v[4:5], 0, v[2:3]
	s_mov_b64 s[0:1], 0x1d800000
	v_lshl_add_u64 v[170:171], v[4:5], 0, s[0:1]
	v_sub_u32_e32 v4, v2, v160
	v_sub_u32_e32 v2, v2, v151
	s_add_i32 s0, 0, 0x20280
	v_lshlrev_b32_e32 v6, 2, v0
	v_lshrrev_b32_e32 v7, 4, v1
	v_add_u32_e32 v2, 0, v2
	v_writelane_b32 v255, s0, 48
	s_mov_b32 s0, 0
	v_lshlrev_b32_e32 v153, 2, v7
	v_cmp_gt_u32_e32 vcc, 16, v1
	v_add_u32_e32 v161, 0, v6
	v_add_u32_e32 v4, 0, v4
	v_add_u32_e32 v182, 0x7c50, v2
	v_mbcnt_lo_u32_b32 v2, -1, 0
	v_writelane_b32 v255, s0, 14
	v_cmp_eq_u32_e64 s[4:5], 0, v1
	v_and_b32_e32 v144, 28, v6
	v_mov_b32_e32 v147, v3
	v_or_b32_e32 v148, 8, v142
	v_or_b32_e32 v150, 16, v142
	v_or_b32_e32 v152, 24, v142
	v_lshl_add_u64 v[156:157], s[14:15], 0, v[154:155]
	v_lshlrev_b32_e32 v158, 5, v149
	v_lshlrev_b32_e32 v162, 3, v7
	v_lshlrev_b32_e32 v159, 2, v149
	v_mov_b32_e32 v167, v3
	v_cndmask_b32_e64 v163, 0, 1.0, vcc
	v_add_u32_e32 v180, 0x5040, v161
	v_add_u32_e32 v181, 0x5420, v4
	v_sub_u32_e32 v183, v153, v149
	s_add_i32 s14, 0, 0x20284
	v_mov_b32_e32 v184, 0xff
	v_mbcnt_hi_u32_b32 v185, -1, v2
	v_mov_b32_e32 v186, 0x1e00000
	v_writelane_b32 v255, s35, 44
	s_branch .LBB0_420

.LBB0_819:
	s_cmp_gt_i32 s81, 3
	s_cselect_b64 s[0:1], -1, 0
	s_and_b64 s[4:5], s[4:5], s[0:1]
	v_readlane_b32 s92, v255, 29
	s_andn2_b64 vcc, exec, s[4:5]
	v_readlane_b32 s89, v255, 28
	v_readlane_b32 s93, v255, 30
	s_cbranch_vccnz .LBB0_871
	s_waitcnt vmcnt(0)
	s_waitcnt vmcnt(0) lgkmcnt(0)
	s_setprio 0
	s_barrier
	s_mov_b64 s[4:5], exec
	v_readlane_b32 s6, v255, 12
	v_readlane_b32 s7, v255, 13
	s_and_b64 s[6:7], s[4:5], s[6:7]
	s_mov_b64 exec, s[6:7]
	s_cbranch_execz .LBB0_870
	s_add_i32 s6, 0, 0x20160
	v_mov_b32_e32 v2, s6
	s_waitcnt vmcnt(0) expcnt(0) lgkmcnt(0)
	ds_read_b32 v4, v2
	s_add_i32 s6, 0, 0x20164
	v_mov_b32_e32 v2, s6
	ds_read_b32 v2, v2
	s_waitcnt lgkmcnt(1)
	v_cmp_ne_u32_e32 vcc, 0, v4
	s_cbranch_vccnz .LBB0_836
	v_readlane_b32 s6, v255, 0
	v_readlane_b32 s7, v255, 1
	v_readlane_b32 s14, v255, 9
	s_load_dwordx2 s[8:9], s[6:7], 0x4
	v_readlane_b32 s15, v255, 10
	s_add_u32 s6, s14, 0x1000
	s_addc_u32 s7, s15, 0
	s_add_u32 s16, s14, 0x1100
	s_addc_u32 s17, s15, 0
	s_add_u32 s18, s14, 0x1200
	v_readlane_b32 s10, v255, 2
	s_addc_u32 s19, s15, 0
	s_waitcnt lgkmcnt(0)
	s_mul_i32 s8, s8, s10
	s_add_u32 s20, s14, 0x1300
	s_mul_i32 s8, s8, s9
	s_addc_u32 s21, s15, 0
	s_mov_b32 s9, 1
	v_mov_b32_e32 v18, 0
	s_branch .LBB0_824
